# baseline (speedup 1.0000x reference)
.LBB3_4:
	s_or_b64 exec, exec, s[8:9]
	v_and_b32_e32 v96, 15, v0
	s_and_b32 s4, s35, 6
	v_mad_u64_u32 v[98:99], s[4:5], s4, 51, v[96:97]
	v_lshrrev_b32_e32 v108, 4, v0
	v_bfe_u32 v99, v0, 4, 2
	s_and_b32 s11, s34, 64
	v_and_b32_e32 v0, 6, v0
	v_or_b32_e32 v1, s11, v96
	v_bitop3_b32 v0, v108, v0, 3 bitop3:0x6c
	v_lshlrev_b32_e32 v1, 7, v1
	v_lshlrev_b32_e32 v0, 4, v0
	v_or_b32_e32 v2, v1, v0
	v_or_b32_e32 v110, 0x14000, v2
	s_mov_b32 s4, 0x14040
	s_waitcnt vmcnt(4) lgkmcnt(0)
	s_barrier
	ds_read_b128 v[40:43], v110
	v_bitop3_b32 v111, v1, s4, v0 bitop3:0x36
	ds_read_b128 v[48:51], v110 offset:2048
	s_lshr_b32 s46, s34, 7
	s_lshr_b32 s47, s46, 1
	s_mul_i32 s47, s47, 0xcc
	s_and_b32 s46, s46, 1
	s_lshl_b32 s46, s46, 4
	s_add_i32 s47, s47, s46
	v_add_u32_e32 v162, s47, v96
	v_lshlrev_b32_e32 v156, 7, v162
	v_bitop3_b32 v155, v162, v99, 6 bitop3:0x6c
	v_lshl_or_b32 v113, v155, 4, v156
	v_add_u32_e32 v157, 51, v162
	v_lshlrev_b32_e32 v156, 7, v157
	v_bitop3_b32 v155, v157, v99, 6 bitop3:0x6c
	v_lshl_or_b32 v114, v155, 4, v156
	v_add_u32_e32 v157, 102, v162
	v_lshlrev_b32_e32 v156, 7, v157
	v_bitop3_b32 v155, v157, v99, 6 bitop3:0x6c
	v_lshl_or_b32 v158, v155, 4, v156
	v_add_u32_e32 v157, 153, v162
	v_lshlrev_b32_e32 v156, 7, v157
	v_bitop3_b32 v155, v157, v99, 6 bitop3:0x6c
	v_lshl_or_b32 v159, v155, 4, v156
	ds_read_b128 v[56:59], v113
	ds_read_b128 v[52:55], v114
	ds_read_b128 v[64:67], v158
	ds_read_b128 v[68:71], v159
	ds_read_b128 v[76:79], v110 offset:4096
	ds_read_b128 v[80:83], v110 offset:6144
	v_mov_b32_e32 v92, 0
	s_lshr_b32 s10, s34, 7
	s_mul_i32 s12, s33, 0x64
	v_lshl_add_u64 v[100:101], v[18:19], 1, s[22:23]
	s_mov_b32 s5, 0
	s_mov_b32 s13, 0xc000
	s_mov_b64 s[8:9], 0x400
	v_mov_b32_e32 v112, 0x64
	s_mov_b32 s14, 0
	v_mov_b32_e32 v93, v92
	v_mov_b32_e32 v94, v92
	v_mov_b32_e32 v95, v92
	v_mov_b32_e32 v88, v92
	v_mov_b32_e32 v89, v92
	v_mov_b32_e32 v90, v92
	v_mov_b32_e32 v91, v92
	v_mov_b32_e32 v84, v92
	v_mov_b32_e32 v85, v92
	v_mov_b32_e32 v86, v92
	v_mov_b32_e32 v87, v92
	v_mov_b32_e32 v72, v92
	v_mov_b32_e32 v73, v92
	v_mov_b32_e32 v74, v92
	v_mov_b32_e32 v75, v92
	v_mov_b32_e32 v60, v92
	v_mov_b32_e32 v61, v92
	v_mov_b32_e32 v62, v92
	v_mov_b32_e32 v63, v92
	v_mov_b32_e32 v44, v92
	v_mov_b32_e32 v45, v92
	v_mov_b32_e32 v46, v92
	v_mov_b32_e32 v47, v92
	v_mov_b32_e32 v36, v92
	v_mov_b32_e32 v37, v92
	v_mov_b32_e32 v38, v92
	v_mov_b32_e32 v39, v92
	v_mov_b32_e32 v32, v92
	v_mov_b32_e32 v33, v92
	v_mov_b32_e32 v34, v92
	v_mov_b32_e32 v35, v92
	v_mov_b32_e32 v28, v92
	v_mov_b32_e32 v29, v92
	v_mov_b32_e32 v30, v92
	v_mov_b32_e32 v31, v92
	v_mov_b32_e32 v24, v92
	v_mov_b32_e32 v25, v92
	v_mov_b32_e32 v26, v92
	v_mov_b32_e32 v27, v92
	v_mov_b32_e32 v20, v92
	v_mov_b32_e32 v21, v92
	v_mov_b32_e32 v22, v92
	v_mov_b32_e32 v23, v92
	v_mov_b32_e32 v16, v92
	v_mov_b32_e32 v17, v92
	v_mov_b32_e32 v18, v92
	v_mov_b32_e32 v19, v92
	v_mov_b32_e32 v12, v92
	v_mov_b32_e32 v13, v92
	v_mov_b32_e32 v14, v92
	v_mov_b32_e32 v15, v92
	v_mov_b32_e32 v8, v92
	v_mov_b32_e32 v9, v92
	v_mov_b32_e32 v10, v92
	v_mov_b32_e32 v11, v92
	v_mov_b32_e32 v4, v92
	v_mov_b32_e32 v5, v92
	v_mov_b32_e32 v6, v92
	v_mov_b32_e32 v7, v92
	v_mov_b32_e32 v0, v92
	v_mov_b32_e32 v1, v92
	v_mov_b32_e32 v2, v92
	v_mov_b32_e32 v3, v92
	s_mov_b32 s40, 1
	s_mov_b32 s41, 1
	v_mov_b32_e32 v115, v111
	s_add_i32 s4, s12, 3
	s_lshl_b32 s4, s4, 14
	v_lshl_add_u64 v[148:149], v[100:101], 0, s[4:5]
	s_add_i32 s42, s27, 0xc000
	v_lshl_add_u64 v[150:151], v[148:149], 0, s[8:9]
	s_mov_b32 s45, 0
	s_waitcnt lgkmcnt(0)
.Lc1_loop:
	s_waitcnt vmcnt(2)
	s_barrier
	s_waitcnt lgkmcnt(5)
	v_mfma_f32_16x16x32_f16 v[92:95], v[40:43], v[56:59], v[92:95]
	ds_read_b128 v[116:119], v115
	v_mfma_f32_16x16x32_f16 v[88:91], v[48:51], v[56:59], v[88:91]
	v_xor_b32_e32 v152, 64, v113
	v_xor_b32_e32 v153, 64, v114
	v_xor_b32_e32 v160, 64, v158
	v_xor_b32_e32 v161, 64, v159
	s_add_i32 s4, s45, 60
	s_add_i32 s4, s4, s12
	s_lshl_b32 s4, s4, 14
	s_waitcnt lgkmcnt(5)
	v_mfma_f32_16x16x32_f16 v[60:63], v[40:43], v[52:55], v[60:63]
	ds_read_b128 v[120:123], v115 offset:2048
	v_lshl_add_u64 v[148:149], v[100:101], 0, s[4:5]
	s_and_b32 s42, s13, 0xc000
	s_add_i32 s42, s42, s27
	v_mfma_f32_16x16x32_f16 v[44:47], v[48:51], v[52:55], v[44:47]
	s_mov_b32 m0, s42
	s_add_i32 s16, s13, 0xffff8000
	global_load_lds_dwordx4 v[148:149], off
	s_waitcnt lgkmcnt(5)
	v_mfma_f32_16x16x32_f16 v[28:31], v[40:43], v[64:67], v[28:31]
	ds_read_b128 v[124:127], v152
	v_mfma_f32_16x16x32_f16 v[24:27], v[48:51], v[64:67], v[24:27]
	s_and_b32 s16, s16, 0xc000
	s_add_i32 s43, s42, 0x400
	v_lshl_add_u64 v[150:151], v[148:149], 0, s[8:9]
	s_waitcnt lgkmcnt(5)
	v_mfma_f32_16x16x32_f16 v[12:15], v[40:43], v[68:71], v[12:15]
	ds_read_b128 v[128:131], v153
	v_mfma_f32_16x16x32_f16 v[8:11], v[48:51], v[68:71], v[8:11]
	v_add_u32_e32 v154, s16, v110
	s_add_i32 s44, s45, 204
	s_waitcnt lgkmcnt(5)
	v_mfma_f32_16x16x32_f16 v[84:87], v[76:79], v[56:59], v[84:87]
	ds_read_b128 v[132:135], v160
	s_waitcnt lgkmcnt(5)
	v_mfma_f32_16x16x32_f16 v[72:75], v[80:83], v[56:59], v[72:75]
	v_add_u32_e32 v157, s44, v162
	v_mfma_f32_16x16x32_f16 v[36:39], v[76:79], v[52:55], v[36:39]
	ds_read_b128 v[136:139], v161
	v_mfma_f32_16x16x32_f16 v[32:35], v[80:83], v[52:55], v[32:35]
	v_lshlrev_b32_e32 v156, 7, v157
	v_bitop3_b32 v155, v157, v99, 6 bitop3:0x6c
	v_mfma_f32_16x16x32_f16 v[20:23], v[76:79], v[64:67], v[20:23]
	ds_read_b128 v[140:143], v115 offset:4096
	v_mfma_f32_16x16x32_f16 v[16:19], v[80:83], v[64:67], v[16:19]
	v_lshl_or_b32 v159, v155, 4, v156
	v_mfma_f32_16x16x32_f16 v[4:7], v[76:79], v[68:71], v[4:7]
	ds_read_b128 v[144:147], v115 offset:6144
	v_mfma_f32_16x16x32_f16 v[0:3], v[80:83], v[68:71], v[0:3]
	v_add_u32_e32 v115, s16, v111
	s_waitcnt lgkmcnt(5)
	v_mfma_f32_16x16x32_f16 v[92:95], v[116:119], v[124:127], v[92:95]
	ds_read_b128 v[40:43], v154
	v_mfma_f32_16x16x32_f16 v[88:91], v[120:123], v[124:127], v[88:91]
	s_mov_b32 m0, s43
	s_addk_i32 s13, 0x4000
	global_load_lds_dwordx4 v[150:151], off
	s_waitcnt lgkmcnt(5)
	v_mfma_f32_16x16x32_f16 v[60:63], v[116:119], v[128:131], v[60:63]
	ds_read_b128 v[48:51], v154 offset:2048
	v_mfma_f32_16x16x32_f16 v[44:47], v[120:123], v[128:131], v[44:47]
	s_waitcnt lgkmcnt(5)
	v_mfma_f32_16x16x32_f16 v[28:31], v[116:119], v[132:135], v[28:31]
	ds_read_b128 v[56:59], v159
	v_mfma_f32_16x16x32_f16 v[24:27], v[120:123], v[132:135], v[24:27]
	s_waitcnt lgkmcnt(5)
	v_mfma_f32_16x16x32_f16 v[12:15], v[116:119], v[136:139], v[12:15]
	v_mfma_f32_16x16x32_f16 v[8:11], v[120:123], v[136:139], v[8:11]
	s_waitcnt lgkmcnt(4)
	v_mfma_f32_16x16x32_f16 v[84:87], v[140:143], v[124:127], v[84:87]
	s_waitcnt lgkmcnt(3)
	v_mfma_f32_16x16x32_f16 v[72:75], v[144:147], v[124:127], v[72:75]
	v_mfma_f32_16x16x32_f16 v[36:39], v[140:143], v[128:131], v[36:39]
	v_mfma_f32_16x16x32_f16 v[32:35], v[144:147], v[128:131], v[32:35]
	v_mfma_f32_16x16x32_f16 v[20:23], v[140:143], v[132:135], v[20:23]
	ds_read_b128 v[76:79], v154 offset:4096
	v_mfma_f32_16x16x32_f16 v[16:19], v[144:147], v[132:135], v[16:19]
	v_mfma_f32_16x16x32_f16 v[4:7], v[140:143], v[136:139], v[4:7]
	ds_read_b128 v[80:83], v154 offset:6144
	v_mfma_f32_16x16x32_f16 v[0:3], v[144:147], v[136:139], v[0:3]
	s_waitcnt vmcnt(2)
	s_barrier
	s_waitcnt lgkmcnt(4)
	v_mfma_f32_16x16x32_f16 v[92:95], v[40:43], v[52:55], v[92:95]
	ds_read_b128 v[116:119], v115
	s_waitcnt lgkmcnt(4)
	v_mfma_f32_16x16x32_f16 v[88:91], v[48:51], v[52:55], v[88:91]
	v_xor_b32_e32 v161, 64, v159
	s_add_i32 s4, s45, 80
	s_add_i32 s4, s4, s12
	s_lshl_b32 s4, s4, 14
	v_mfma_f32_16x16x32_f16 v[60:63], v[40:43], v[64:67], v[60:63]
	ds_read_b128 v[120:123], v115 offset:2048
	v_lshl_add_u64 v[148:149], v[100:101], 0, s[4:5]
	s_and_b32 s42, s13, 0xc000
	s_add_i32 s42, s42, s27
	v_mfma_f32_16x16x32_f16 v[44:47], v[48:51], v[64:67], v[44:47]
	s_mov_b32 m0, s42
	s_add_i32 s16, s13, 0xffff8000
	global_load_lds_dwordx4 v[148:149], off
	v_mfma_f32_16x16x32_f16 v[28:31], v[40:43], v[68:71], v[28:31]
	ds_read_b128 v[124:127], v161
	v_mfma_f32_16x16x32_f16 v[24:27], v[48:51], v[68:71], v[24:27]
	s_and_b32 s16, s16, 0xc000
	s_add_i32 s43, s42, 0x400
	v_lshl_add_u64 v[150:151], v[148:149], 0, s[8:9]
	s_waitcnt lgkmcnt(5)
	v_mfma_f32_16x16x32_f16 v[12:15], v[40:43], v[56:59], v[12:15]
	v_mfma_f32_16x16x32_f16 v[8:11], v[48:51], v[56:59], v[8:11]
	v_add_u32_e32 v154, s16, v110
	s_add_i32 s44, s45, 255
	s_waitcnt lgkmcnt(4)
	v_mfma_f32_16x16x32_f16 v[84:87], v[76:79], v[52:55], v[84:87]
	s_waitcnt lgkmcnt(3)
	v_mfma_f32_16x16x32_f16 v[72:75], v[80:83], v[52:55], v[72:75]
	v_add_u32_e32 v157, s44, v162
	v_mfma_f32_16x16x32_f16 v[36:39], v[76:79], v[64:67], v[36:39]
	v_mfma_f32_16x16x32_f16 v[32:35], v[80:83], v[64:67], v[32:35]
	v_lshlrev_b32_e32 v156, 7, v157
	v_bitop3_b32 v155, v157, v99, 6 bitop3:0x6c
	v_mfma_f32_16x16x32_f16 v[20:23], v[76:79], v[68:71], v[20:23]
	ds_read_b128 v[140:143], v115 offset:4096
	v_mfma_f32_16x16x32_f16 v[16:19], v[80:83], v[68:71], v[16:19]
	v_lshl_or_b32 v159, v155, 4, v156
	v_mfma_f32_16x16x32_f16 v[4:7], v[76:79], v[56:59], v[4:7]
	ds_read_b128 v[144:147], v115 offset:6144
	v_mfma_f32_16x16x32_f16 v[0:3], v[80:83], v[56:59], v[0:3]
	v_add_u32_e32 v115, s16, v111
	s_waitcnt lgkmcnt(4)
	v_mfma_f32_16x16x32_f16 v[92:95], v[116:119], v[128:131], v[92:95]
	ds_read_b128 v[40:43], v154
	s_waitcnt lgkmcnt(4)
	v_mfma_f32_16x16x32_f16 v[88:91], v[120:123], v[128:131], v[88:91]
	s_mov_b32 m0, s43
	s_addk_i32 s13, 0x4000
	global_load_lds_dwordx4 v[150:151], off
	v_mfma_f32_16x16x32_f16 v[60:63], v[116:119], v[132:135], v[60:63]
	ds_read_b128 v[48:51], v154 offset:2048
	v_mfma_f32_16x16x32_f16 v[44:47], v[120:123], v[132:135], v[44:47]
	v_mfma_f32_16x16x32_f16 v[28:31], v[116:119], v[136:139], v[28:31]
	ds_read_b128 v[52:55], v159
	v_mfma_f32_16x16x32_f16 v[24:27], v[120:123], v[136:139], v[24:27]
	s_waitcnt lgkmcnt(5)
	v_mfma_f32_16x16x32_f16 v[12:15], v[116:119], v[124:127], v[12:15]
	v_mfma_f32_16x16x32_f16 v[8:11], v[120:123], v[124:127], v[8:11]
	s_waitcnt lgkmcnt(4)
	v_mfma_f32_16x16x32_f16 v[84:87], v[140:143], v[128:131], v[84:87]
	s_waitcnt lgkmcnt(3)
	v_mfma_f32_16x16x32_f16 v[72:75], v[144:147], v[128:131], v[72:75]
	v_mfma_f32_16x16x32_f16 v[36:39], v[140:143], v[132:135], v[36:39]
	v_mfma_f32_16x16x32_f16 v[32:35], v[144:147], v[132:135], v[32:35]
	v_mfma_f32_16x16x32_f16 v[20:23], v[140:143], v[136:139], v[20:23]
	ds_read_b128 v[76:79], v154 offset:4096
	v_mfma_f32_16x16x32_f16 v[16:19], v[144:147], v[136:139], v[16:19]
	v_mfma_f32_16x16x32_f16 v[4:7], v[140:143], v[124:127], v[4:7]
	ds_read_b128 v[80:83], v154 offset:6144
	v_mfma_f32_16x16x32_f16 v[0:3], v[144:147], v[124:127], v[0:3]
	s_waitcnt vmcnt(2)
	s_barrier
	s_waitcnt lgkmcnt(4)
	v_mfma_f32_16x16x32_f16 v[92:95], v[40:43], v[64:67], v[92:95]
	ds_read_b128 v[116:119], v115
	s_waitcnt lgkmcnt(4)
	v_mfma_f32_16x16x32_f16 v[88:91], v[48:51], v[64:67], v[88:91]
	v_xor_b32_e32 v161, 64, v159
	s_add_i32 s4, s45, 1
	s_add_i32 s4, s4, s12
	s_lshl_b32 s4, s4, 14
	v_mfma_f32_16x16x32_f16 v[60:63], v[40:43], v[68:71], v[60:63]
	ds_read_b128 v[120:123], v115 offset:2048
	v_lshl_add_u64 v[148:149], v[100:101], 0, s[4:5]
	s_and_b32 s42, s13, 0xc000
	s_add_i32 s42, s42, s27
	v_mfma_f32_16x16x32_f16 v[44:47], v[48:51], v[68:71], v[44:47]
	s_mov_b32 m0, s42
	s_add_i32 s16, s13, 0xffff8000
	global_load_lds_dwordx4 v[148:149], off
	v_mfma_f32_16x16x32_f16 v[28:31], v[40:43], v[56:59], v[28:31]
	ds_read_b128 v[128:131], v161
	v_mfma_f32_16x16x32_f16 v[24:27], v[48:51], v[56:59], v[24:27]
	s_and_b32 s16, s16, 0xc000
	s_add_i32 s43, s42, 0x400
	v_lshl_add_u64 v[150:151], v[148:149], 0, s[8:9]
	s_waitcnt lgkmcnt(5)
	v_mfma_f32_16x16x32_f16 v[12:15], v[40:43], v[52:55], v[12:15]
	v_mfma_f32_16x16x32_f16 v[8:11], v[48:51], v[52:55], v[8:11]
	v_add_u32_e32 v154, s16, v110
	s_add_i32 s44, s45, 306
	s_waitcnt lgkmcnt(4)
	v_mfma_f32_16x16x32_f16 v[84:87], v[76:79], v[64:67], v[84:87]
	s_waitcnt lgkmcnt(3)
	v_mfma_f32_16x16x32_f16 v[72:75], v[80:83], v[64:67], v[72:75]
	v_add_u32_e32 v157, s44, v162
	v_mfma_f32_16x16x32_f16 v[36:39], v[76:79], v[68:71], v[36:39]
	v_mfma_f32_16x16x32_f16 v[32:35], v[80:83], v[68:71], v[32:35]
	v_lshlrev_b32_e32 v156, 7, v157
	v_bitop3_b32 v155, v157, v99, 6 bitop3:0x6c
	v_mfma_f32_16x16x32_f16 v[20:23], v[76:79], v[56:59], v[20:23]
	ds_read_b128 v[140:143], v115 offset:4096
	v_mfma_f32_16x16x32_f16 v[16:19], v[80:83], v[56:59], v[16:19]
	v_lshl_or_b32 v159, v155, 4, v156
	v_mfma_f32_16x16x32_f16 v[4:7], v[76:79], v[52:55], v[4:7]
	ds_read_b128 v[144:147], v115 offset:6144
	v_mfma_f32_16x16x32_f16 v[0:3], v[80:83], v[52:55], v[0:3]
	v_add_u32_e32 v115, s16, v111
	s_waitcnt lgkmcnt(4)
	v_mfma_f32_16x16x32_f16 v[92:95], v[116:119], v[132:135], v[92:95]
	ds_read_b128 v[40:43], v154
	s_waitcnt lgkmcnt(4)
	v_mfma_f32_16x16x32_f16 v[88:91], v[120:123], v[132:135], v[88:91]
	s_mov_b32 m0, s43
	s_addk_i32 s13, 0x4000
	global_load_lds_dwordx4 v[150:151], off
	v_mfma_f32_16x16x32_f16 v[60:63], v[116:119], v[136:139], v[60:63]
	ds_read_b128 v[48:51], v154 offset:2048
	v_mfma_f32_16x16x32_f16 v[44:47], v[120:123], v[136:139], v[44:47]
	v_mfma_f32_16x16x32_f16 v[28:31], v[116:119], v[124:127], v[28:31]
	ds_read_b128 v[64:67], v159
	v_mfma_f32_16x16x32_f16 v[24:27], v[120:123], v[124:127], v[24:27]
	s_waitcnt lgkmcnt(5)
	v_mfma_f32_16x16x32_f16 v[12:15], v[116:119], v[128:131], v[12:15]
	v_mfma_f32_16x16x32_f16 v[8:11], v[120:123], v[128:131], v[8:11]
	s_waitcnt lgkmcnt(4)
	v_mfma_f32_16x16x32_f16 v[84:87], v[140:143], v[132:135], v[84:87]
	s_waitcnt lgkmcnt(3)
	v_mfma_f32_16x16x32_f16 v[72:75], v[144:147], v[132:135], v[72:75]
	v_mfma_f32_16x16x32_f16 v[36:39], v[140:143], v[136:139], v[36:39]
	v_mfma_f32_16x16x32_f16 v[32:35], v[144:147], v[136:139], v[32:35]
	v_mfma_f32_16x16x32_f16 v[20:23], v[140:143], v[124:127], v[20:23]
	ds_read_b128 v[76:79], v154 offset:4096
	v_mfma_f32_16x16x32_f16 v[16:19], v[144:147], v[124:127], v[16:19]
	v_mfma_f32_16x16x32_f16 v[4:7], v[140:143], v[128:131], v[4:7]
	ds_read_b128 v[80:83], v154 offset:6144
	v_mfma_f32_16x16x32_f16 v[0:3], v[144:147], v[128:131], v[0:3]
	s_waitcnt vmcnt(2)
	s_barrier
	s_waitcnt lgkmcnt(4)
	v_mfma_f32_16x16x32_f16 v[92:95], v[40:43], v[68:71], v[92:95]
	ds_read_b128 v[116:119], v115
	s_waitcnt lgkmcnt(4)
	v_mfma_f32_16x16x32_f16 v[88:91], v[48:51], v[68:71], v[88:91]
	v_xor_b32_e32 v161, 64, v159
	s_add_i32 s4, s45, 21
	s_add_i32 s4, s4, s12
	s_lshl_b32 s4, s4, 14
	v_mfma_f32_16x16x32_f16 v[60:63], v[40:43], v[56:59], v[60:63]
	ds_read_b128 v[120:123], v115 offset:2048
	v_lshl_add_u64 v[148:149], v[100:101], 0, s[4:5]
	s_and_b32 s42, s13, 0xc000
	s_add_i32 s42, s42, s27
	v_mfma_f32_16x16x32_f16 v[44:47], v[48:51], v[56:59], v[44:47]
	s_mov_b32 m0, s42
	s_add_i32 s16, s13, 0xffff8000
	global_load_lds_dwordx4 v[148:149], off
	v_mfma_f32_16x16x32_f16 v[28:31], v[40:43], v[52:55], v[28:31]
	ds_read_b128 v[132:135], v161
	v_mfma_f32_16x16x32_f16 v[24:27], v[48:51], v[52:55], v[24:27]
	s_and_b32 s16, s16, 0xc000
	s_add_i32 s43, s42, 0x400
	v_lshl_add_u64 v[150:151], v[148:149], 0, s[8:9]
	s_waitcnt lgkmcnt(5)
	v_mfma_f32_16x16x32_f16 v[12:15], v[40:43], v[64:67], v[12:15]
	v_mfma_f32_16x16x32_f16 v[8:11], v[48:51], v[64:67], v[8:11]
	v_add_u32_e32 v154, s16, v110
	s_add_i32 s44, s45, 357
	s_waitcnt lgkmcnt(4)
	v_mfma_f32_16x16x32_f16 v[84:87], v[76:79], v[68:71], v[84:87]
	s_waitcnt lgkmcnt(3)
	v_mfma_f32_16x16x32_f16 v[72:75], v[80:83], v[68:71], v[72:75]
	v_add_u32_e32 v157, s44, v162
	v_mfma_f32_16x16x32_f16 v[36:39], v[76:79], v[56:59], v[36:39]
	v_mfma_f32_16x16x32_f16 v[32:35], v[80:83], v[56:59], v[32:35]
	v_lshlrev_b32_e32 v156, 7, v157
	v_bitop3_b32 v155, v157, v99, 6 bitop3:0x6c
	v_mfma_f32_16x16x32_f16 v[20:23], v[76:79], v[52:55], v[20:23]
	ds_read_b128 v[140:143], v115 offset:4096
	v_mfma_f32_16x16x32_f16 v[16:19], v[80:83], v[52:55], v[16:19]
	v_lshl_or_b32 v159, v155, 4, v156
	v_mfma_f32_16x16x32_f16 v[4:7], v[76:79], v[64:67], v[4:7]
	ds_read_b128 v[144:147], v115 offset:6144
	v_mfma_f32_16x16x32_f16 v[0:3], v[80:83], v[64:67], v[0:3]
	v_add_u32_e32 v115, s16, v111
	s_waitcnt lgkmcnt(4)
	v_mfma_f32_16x16x32_f16 v[92:95], v[116:119], v[136:139], v[92:95]
	ds_read_b128 v[40:43], v154
	s_waitcnt lgkmcnt(4)
	v_mfma_f32_16x16x32_f16 v[88:91], v[120:123], v[136:139], v[88:91]
	s_mov_b32 m0, s43
	s_addk_i32 s13, 0x4000
	global_load_lds_dwordx4 v[150:151], off
	v_mfma_f32_16x16x32_f16 v[60:63], v[116:119], v[124:127], v[60:63]
	ds_read_b128 v[48:51], v154 offset:2048
	v_mfma_f32_16x16x32_f16 v[44:47], v[120:123], v[124:127], v[44:47]
	v_mfma_f32_16x16x32_f16 v[28:31], v[116:119], v[128:131], v[28:31]
	ds_read_b128 v[68:71], v159
	v_mfma_f32_16x16x32_f16 v[24:27], v[120:123], v[128:131], v[24:27]
	s_waitcnt lgkmcnt(5)
	v_mfma_f32_16x16x32_f16 v[12:15], v[116:119], v[132:135], v[12:15]
	v_mfma_f32_16x16x32_f16 v[8:11], v[120:123], v[132:135], v[8:11]
	s_waitcnt lgkmcnt(4)
	v_mfma_f32_16x16x32_f16 v[84:87], v[140:143], v[136:139], v[84:87]
	s_waitcnt lgkmcnt(3)
	v_mfma_f32_16x16x32_f16 v[72:75], v[144:147], v[136:139], v[72:75]
	v_mfma_f32_16x16x32_f16 v[36:39], v[140:143], v[124:127], v[36:39]
	v_mfma_f32_16x16x32_f16 v[32:35], v[144:147], v[124:127], v[32:35]
	v_mfma_f32_16x16x32_f16 v[20:23], v[140:143], v[128:131], v[20:23]
	ds_read_b128 v[76:79], v154 offset:4096
	v_mfma_f32_16x16x32_f16 v[16:19], v[144:147], v[128:131], v[16:19]
	v_mfma_f32_16x16x32_f16 v[4:7], v[140:143], v[132:135], v[4:7]
	ds_read_b128 v[80:83], v154 offset:6144
	v_mfma_f32_16x16x32_f16 v[0:3], v[144:147], v[132:135], v[0:3]
	s_waitcnt vmcnt(2)
	s_barrier
	s_waitcnt lgkmcnt(4)
	v_mfma_f32_16x16x32_f16 v[92:95], v[40:43], v[56:59], v[92:95]
	ds_read_b128 v[116:119], v115
	s_waitcnt lgkmcnt(4)
	v_mfma_f32_16x16x32_f16 v[88:91], v[48:51], v[56:59], v[88:91]
	v_xor_b32_e32 v161, 64, v159
	s_add_i32 s4, s45, 41
	s_add_i32 s4, s4, s12
	s_lshl_b32 s4, s4, 14
	v_mfma_f32_16x16x32_f16 v[60:63], v[40:43], v[52:55], v[60:63]
	ds_read_b128 v[120:123], v115 offset:2048
	v_lshl_add_u64 v[148:149], v[100:101], 0, s[4:5]
	s_and_b32 s42, s13, 0xc000
	s_add_i32 s42, s42, s27
	v_mfma_f32_16x16x32_f16 v[44:47], v[48:51], v[52:55], v[44:47]
	s_mov_b32 m0, s42
	s_add_i32 s16, s13, 0xffff8000
	global_load_lds_dwordx4 v[148:149], off
	v_mfma_f32_16x16x32_f16 v[28:31], v[40:43], v[64:67], v[28:31]
	ds_read_b128 v[136:139], v161
	v_mfma_f32_16x16x32_f16 v[24:27], v[48:51], v[64:67], v[24:27]
	s_and_b32 s16, s16, 0xc000
	s_add_i32 s43, s42, 0x400
	v_lshl_add_u64 v[150:151], v[148:149], 0, s[8:9]
	s_waitcnt lgkmcnt(5)
	v_mfma_f32_16x16x32_f16 v[12:15], v[40:43], v[68:71], v[12:15]
	v_mfma_f32_16x16x32_f16 v[8:11], v[48:51], v[68:71], v[8:11]
	v_add_u32_e32 v154, s16, v110
	s_add_i32 s44, s45, 1
	s_waitcnt lgkmcnt(4)
	v_mfma_f32_16x16x32_f16 v[84:87], v[76:79], v[56:59], v[84:87]
	v_add_u32_e32 v157, s44, v162
	s_waitcnt lgkmcnt(3)
	v_mfma_f32_16x16x32_f16 v[72:75], v[80:83], v[56:59], v[72:75]
	v_lshlrev_b32_e32 v156, 7, v157
	v_bitop3_b32 v155, v157, v99, 6 bitop3:0x6c
	v_lshl_or_b32 v113, v155, 4, v156
	v_mfma_f32_16x16x32_f16 v[36:39], v[76:79], v[52:55], v[36:39]
	v_add_u32_e32 v157, 51, v157
	v_mfma_f32_16x16x32_f16 v[32:35], v[80:83], v[52:55], v[32:35]
	v_lshlrev_b32_e32 v156, 7, v157
	v_bitop3_b32 v155, v157, v99, 6 bitop3:0x6c
	v_lshl_or_b32 v114, v155, 4, v156
	v_mfma_f32_16x16x32_f16 v[20:23], v[76:79], v[64:67], v[20:23]
	ds_read_b128 v[140:143], v115 offset:4096
	v_add_u32_e32 v157, 51, v157
	v_mfma_f32_16x16x32_f16 v[16:19], v[80:83], v[64:67], v[16:19]
	v_lshlrev_b32_e32 v156, 7, v157
	v_bitop3_b32 v155, v157, v99, 6 bitop3:0x6c
	v_lshl_or_b32 v158, v155, 4, v156
	v_mfma_f32_16x16x32_f16 v[4:7], v[76:79], v[68:71], v[4:7]
	ds_read_b128 v[144:147], v115 offset:6144
	v_add_u32_e32 v157, 51, v157
	v_mfma_f32_16x16x32_f16 v[0:3], v[80:83], v[68:71], v[0:3]
	v_add_u32_e32 v115, s16, v111
	s_waitcnt lgkmcnt(4)
	v_mfma_f32_16x16x32_f16 v[92:95], v[116:119], v[124:127], v[92:95]
	ds_read_b128 v[40:43], v154
	v_lshlrev_b32_e32 v156, 7, v157
	v_bitop3_b32 v155, v157, v99, 6 bitop3:0x6c
	v_lshl_or_b32 v159, v155, 4, v156
	s_waitcnt lgkmcnt(4)
	v_mfma_f32_16x16x32_f16 v[88:91], v[120:123], v[124:127], v[88:91]
	s_mov_b32 m0, s43
	s_addk_i32 s13, 0x4000
	global_load_lds_dwordx4 v[150:151], off
	v_mfma_f32_16x16x32_f16 v[60:63], v[116:119], v[128:131], v[60:63]
	ds_read_b128 v[48:51], v154 offset:2048
	v_mfma_f32_16x16x32_f16 v[44:47], v[120:123], v[128:131], v[44:47]
	v_mfma_f32_16x16x32_f16 v[28:31], v[116:119], v[132:135], v[28:31]
	ds_read_b128 v[56:59], v113
	v_mfma_f32_16x16x32_f16 v[24:27], v[120:123], v[132:135], v[24:27]
	s_waitcnt lgkmcnt(5)
	v_mfma_f32_16x16x32_f16 v[12:15], v[116:119], v[136:139], v[12:15]
	ds_read_b128 v[52:55], v114
	v_mfma_f32_16x16x32_f16 v[8:11], v[120:123], v[136:139], v[8:11]
	s_waitcnt lgkmcnt(5)
	v_mfma_f32_16x16x32_f16 v[84:87], v[140:143], v[124:127], v[84:87]
	ds_read_b128 v[64:67], v158
	s_waitcnt lgkmcnt(5)
	v_mfma_f32_16x16x32_f16 v[72:75], v[144:147], v[124:127], v[72:75]
	v_mfma_f32_16x16x32_f16 v[36:39], v[140:143], v[128:131], v[36:39]
	ds_read_b128 v[68:71], v159
	v_mfma_f32_16x16x32_f16 v[32:35], v[144:147], v[128:131], v[32:35]
	v_mfma_f32_16x16x32_f16 v[20:23], v[140:143], v[132:135], v[20:23]
	ds_read_b128 v[76:79], v154 offset:4096
	v_mfma_f32_16x16x32_f16 v[16:19], v[144:147], v[132:135], v[16:19]
	s_add_i32 s45, s45, 1
	v_mfma_f32_16x16x32_f16 v[4:7], v[140:143], v[136:139], v[4:7]
	ds_read_b128 v[80:83], v154 offset:6144
	s_cmp_eq_u32 s45, 20
	v_mfma_f32_16x16x32_f16 v[0:3], v[144:147], v[136:139], v[0:3]
	s_cbranch_scc0 .Lc1_loop
	s_waitcnt vmcnt(0) lgkmcnt(0)
	s_cmpk_gt_u32 s34, 0x1ff
	s_barrier
	s_cbranch_scc1 .LBB3_8
	s_load_dword s0, s[0:1], 0x38
	s_lshr_b32 s46, s10, 1
	s_lshl_b32 s46, s46, 7
	s_and_b32 s47, s10, 1
	s_lshl_b32 s47, s47, 4
	s_or_b32 s46, s46, s47
	v_or_b32_e32 v40, s46, v96
	s_movk_i32 s4, 0x110
	v_lshlrev_b32_e32 v41, 3, v99
	s_lshl_b32 s1, s11, 1
	v_mul_lo_u32 v40, v40, s4
	v_add3_u32 v48, s1, v41, v40
	v_mov_b32_e32 v40, v93
	v_mov_b32_e32 v41, v94
	s_waitcnt lgkmcnt(0)
	v_pk_mul_f32 v[40:41], s[0:1], v[40:41] op_sel_hi:[0,1]
	v_fma_mixlo_f16 v42, s0, v92, 0
	v_cvt_pk_f16_f32 v41, v40, v41
	v_pack_b32_f16 v40, v42, v41
	v_fma_mixlo_f16 v42, s0, v95, 0
	v_alignbit_b32 v41, v42, v41, 16
	v_mov_b32_e32 v42, v89
	v_mov_b32_e32 v43, v90
	v_pk_mul_f32 v[42:43], s[0:1], v[42:43] op_sel_hi:[0,1]
	v_fma_mixlo_f16 v49, s0, v88, 0
	v_cvt_pk_f16_f32 v43, v42, v43
	v_pack_b32_f16 v42, v49, v43
	v_fma_mixlo_f16 v49, s0, v91, 0
	v_alignbit_b32 v43, v49, v43, 16
	ds_write2_b64 v48, v[40:41], v[42:43] offset1:4
	v_mov_b32_e32 v40, v85
	v_mov_b32_e32 v41, v86
	v_pk_mul_f32 v[40:41], s[0:1], v[40:41] op_sel_hi:[0,1]
	v_fma_mixlo_f16 v42, s0, v84, 0
	v_cvt_pk_f16_f32 v41, v40, v41
	v_pack_b32_f16 v40, v42, v41
	v_fma_mixlo_f16 v42, s0, v87, 0
	v_alignbit_b32 v41, v42, v41, 16
	v_mov_b32_e32 v42, v73
	v_mov_b32_e32 v43, v74
	v_pk_mul_f32 v[42:43], s[0:1], v[42:43] op_sel_hi:[0,1]
	v_fma_mixlo_f16 v49, s0, v72, 0
	v_cvt_pk_f16_f32 v43, v42, v43
	v_pack_b32_f16 v42, v49, v43
	v_fma_mixlo_f16 v49, s0, v75, 0
	v_alignbit_b32 v43, v49, v43, 16
	ds_write2_b64 v48, v[40:41], v[42:43] offset0:8 offset1:12
	v_mov_b32_e32 v40, v61
	v_mov_b32_e32 v41, v62
	v_pk_mul_f32 v[40:41], s[0:1], v[40:41] op_sel_hi:[0,1]
	v_fma_mixlo_f16 v42, s0, v60, 0
	v_cvt_pk_f16_f32 v41, v40, v41
	v_pack_b32_f16 v40, v42, v41
	v_fma_mixlo_f16 v42, s0, v63, 0
	v_alignbit_b32 v41, v42, v41, 16
	v_mov_b32_e32 v42, v45
	v_mov_b32_e32 v43, v46
	v_pk_mul_f32 v[42:43], s[0:1], v[42:43] op_sel_hi:[0,1]
	v_fma_mixlo_f16 v44, s0, v44, 0
	v_cvt_pk_f16_f32 v43, v42, v43
	v_pack_b32_f16 v42, v44, v43
	v_fma_mixlo_f16 v44, s0, v47, 0
	v_alignbit_b32 v43, v44, v43, 16
	v_add_u32_e32 v44, 0x2100, v48
	ds_write2_b64 v44, v[40:41], v[42:43] offset0:32 offset1:36
	v_fma_mixlo_f16 v40, s0, v36, 0
	v_mov_b32_e32 v36, v37
	v_mov_b32_e32 v37, v38
	v_pk_mul_f32 v[36:37], s[0:1], v[36:37] op_sel_hi:[0,1]
	v_cvt_pk_f16_f32 v37, v36, v37
	v_fma_mixlo_f16 v38, s0, v39, 0
	v_pack_b32_f16 v36, v40, v37
	v_alignbit_b32 v37, v38, v37, 16
	v_fma_mixlo_f16 v38, s0, v32, 0
	v_mov_b32_e32 v32, v33
	v_mov_b32_e32 v33, v34
	v_pk_mul_f32 v[32:33], s[0:1], v[32:33] op_sel_hi:[0,1]
	v_cvt_pk_f16_f32 v33, v32, v33
	v_fma_mixlo_f16 v34, s0, v35, 0
	v_pack_b32_f16 v32, v38, v33
	v_alignbit_b32 v33, v34, v33, 16
	ds_write2_b64 v44, v[36:37], v[32:33] offset0:40 offset1:44
	v_fma_mixlo_f16 v32, s0, v28, 0
	v_mov_b32_e32 v28, v29
	v_mov_b32_e32 v29, v30
	v_pk_mul_f32 v[28:29], s[0:1], v[28:29] op_sel_hi:[0,1]
	v_cvt_pk_f16_f32 v29, v28, v29
	v_fma_mixlo_f16 v30, s0, v31, 0
	v_pack_b32_f16 v28, v32, v29
	v_alignbit_b32 v29, v30, v29, 16
	v_fma_mixlo_f16 v30, s0, v24, 0
	v_mov_b32_e32 v24, v25
	v_mov_b32_e32 v25, v26
	v_pk_mul_f32 v[24:25], s[0:1], v[24:25] op_sel_hi:[0,1]
	v_cvt_pk_f16_f32 v25, v24, v25
	v_fma_mixlo_f16 v26, s0, v27, 0
	v_pack_b32_f16 v24, v30, v25
	v_alignbit_b32 v25, v26, v25, 16
	v_add_u32_e32 v26, 0x4200, v48
	ds_write2_b64 v26, v[28:29], v[24:25] offset0:64 offset1:68
	v_fma_mixlo_f16 v24, s0, v20, 0
	v_mov_b32_e32 v20, v21
	v_mov_b32_e32 v21, v22
	v_pk_mul_f32 v[20:21], s[0:1], v[20:21] op_sel_hi:[0,1]
	v_cvt_pk_f16_f32 v21, v20, v21
	v_fma_mixlo_f16 v22, s0, v23, 0
	v_pack_b32_f16 v20, v24, v21
	v_alignbit_b32 v21, v22, v21, 16
	v_fma_mixlo_f16 v22, s0, v16, 0
	v_mov_b32_e32 v16, v17
	v_mov_b32_e32 v17, v18
	v_pk_mul_f32 v[16:17], s[0:1], v[16:17] op_sel_hi:[0,1]
	v_cvt_pk_f16_f32 v17, v16, v17
	v_fma_mixlo_f16 v18, s0, v19, 0
	v_pack_b32_f16 v16, v22, v17
	v_alignbit_b32 v17, v18, v17, 16
	ds_write2_b64 v26, v[20:21], v[16:17] offset0:72 offset1:76
	v_fma_mixlo_f16 v16, s0, v12, 0
	v_mov_b32_e32 v12, v13
	v_mov_b32_e32 v13, v14
	v_pk_mul_f32 v[12:13], s[0:1], v[12:13] op_sel_hi:[0,1]
	v_cvt_pk_f16_f32 v13, v12, v13
	v_fma_mixlo_f16 v14, s0, v15, 0
	v_pack_b32_f16 v12, v16, v13
	v_alignbit_b32 v13, v14, v13, 16
	v_fma_mixlo_f16 v14, s0, v8, 0
	v_mov_b32_e32 v8, v9
	v_mov_b32_e32 v9, v10
	v_pk_mul_f32 v[8:9], s[0:1], v[8:9] op_sel_hi:[0,1]
	v_cvt_pk_f16_f32 v9, v8, v9
	v_fma_mixlo_f16 v10, s0, v11, 0
	v_pack_b32_f16 v8, v14, v9
	v_alignbit_b32 v9, v10, v9, 16
	v_add_u32_e32 v10, 0x6300, v48
	ds_write2_b64 v10, v[12:13], v[8:9] offset0:96 offset1:100
	v_fma_mixlo_f16 v8, s0, v4, 0
	v_mov_b32_e32 v4, v5
	v_mov_b32_e32 v5, v6
	v_pk_mul_f32 v[4:5], s[0:1], v[4:5] op_sel_hi:[0,1]
	v_cvt_pk_f16_f32 v5, v4, v5
	v_fma_mixlo_f16 v6, s0, v7, 0
	v_pack_b32_f16 v4, v8, v5
	v_alignbit_b32 v5, v6, v5, 16
	v_fma_mixlo_f16 v6, s0, v0, 0
	v_mov_b32_e32 v0, v1
	v_mov_b32_e32 v1, v2
	v_pk_mul_f32 v[0:1], s[0:1], v[0:1] op_sel_hi:[0,1]
	v_cvt_pk_f16_f32 v1, v0, v1
	v_fma_mixlo_f16 v2, s0, v3, 0
	v_pack_b32_f16 v0, v6, v1
	v_alignbit_b32 v1, v2, v1, 16
	ds_write2_b64 v10, v[4:5], v[0:1] offset0:104 offset1:108

	.amdhsa_kernel _Z6conv_kILi64ELi128ELi20ELi128ELi4ELi4ELb1EEvPKDF16_S1_PKfS3_PDF16_S4_S1_fS3_S3_S3_S3_
		.amdhsa_group_segment_fixed_size 147456
		.amdhsa_private_segment_fixed_size 0
		.amdhsa_kernarg_size 96
		.amdhsa_user_sgpr_count 2
		.amdhsa_user_sgpr_dispatch_ptr 0
		.amdhsa_user_sgpr_queue_ptr 0
		.amdhsa_user_sgpr_kernarg_segment_ptr 1
		.amdhsa_user_sgpr_dispatch_id 0
		.amdhsa_user_sgpr_kernarg_preload_length 0
		.amdhsa_user_sgpr_kernarg_preload_offset 0
		.amdhsa_user_sgpr_private_segment_size 0
		.amdhsa_uses_dynamic_stack 0
		.amdhsa_enable_private_segment 0
		.amdhsa_system_sgpr_workgroup_id_x 1
		.amdhsa_system_sgpr_workgroup_id_y 0
		.amdhsa_system_sgpr_workgroup_id_z 0
		.amdhsa_system_sgpr_workgroup_info 0
		.amdhsa_system_vgpr_workitem_id 0
		.amdhsa_next_free_vgpr 169
		.amdhsa_next_free_sgpr 96
		.amdhsa_accum_offset 164
		.amdhsa_reserve_vcc 1
		.amdhsa_float_round_mode_32 0
		.amdhsa_float_round_mode_16_64 0
		.amdhsa_float_denorm_mode_32 3
		.amdhsa_float_denorm_mode_16_64 3
		.amdhsa_dx10_clamp 1
		.amdhsa_ieee_mode 1
		.amdhsa_fp16_overflow 0
		.amdhsa_tg_split 0
		.amdhsa_exception_fp_ieee_invalid_op 0
		.amdhsa_exception_fp_denorm_src 0
		.amdhsa_exception_fp_ieee_div_zero 0
		.amdhsa_exception_fp_ieee_overflow 0
		.amdhsa_exception_fp_ieee_underflow 0
		.amdhsa_exception_fp_ieee_inexact 0
		.amdhsa_exception_int_div_zero 0
	.end_amdhsa_kernel

amdhsa.kernels:
  - .agpr_count:     0
    .args:
      - .actual_access:  read_only
        .address_space:  global
        .offset:         0
        .size:           8
        .value_kind:     global_buffer
      - .actual_access:  read_only
        .address_space:  global
        .offset:         8
        .size:           8
        .value_kind:     global_buffer
      - .actual_access:  read_only
        .address_space:  global
        .offset:         16
        .size:           8
        .value_kind:     global_buffer
      - .actual_access:  read_only
        .address_space:  global
        .offset:         24
        .size:           8
        .value_kind:     global_buffer
      - .actual_access:  read_only
        .address_space:  global
        .offset:         32
        .size:           8
        .value_kind:     global_buffer
      - .actual_access:  read_only
        .address_space:  global
        .offset:         40
        .size:           8
        .value_kind:     global_buffer
      - .actual_access:  write_only
        .address_space:  global
        .offset:         48
        .size:           8
        .value_kind:     global_buffer
      - .actual_access:  write_only
        .address_space:  global
        .offset:         56
        .size:           8
        .value_kind:     global_buffer
      - .actual_access:  write_only
        .address_space:  global
        .offset:         64
        .size:           8
        .value_kind:     global_buffer
      - .actual_access:  write_only
        .address_space:  global
        .offset:         72
        .size:           8
        .value_kind:     global_buffer
      - .actual_access:  write_only
        .address_space:  global
        .offset:         80
        .size:           8
        .value_kind:     global_buffer
      - .actual_access:  write_only
        .address_space:  global
        .offset:         88
        .size:           8
        .value_kind:     global_buffer
      - .actual_access:  read_only
        .address_space:  global
        .offset:         96
        .size:           8
        .value_kind:     global_buffer
      - .actual_access:  read_only
        .address_space:  global
        .offset:         104
        .size:           8
        .value_kind:     global_buffer
      - .actual_access:  read_only
        .address_space:  global
        .offset:         112
        .size:           8
        .value_kind:     global_buffer
      - .actual_access:  read_only
        .address_space:  global
        .offset:         120
        .size:           8
        .value_kind:     global_buffer
      - .actual_access:  write_only
        .address_space:  global
        .offset:         128
        .size:           8
        .value_kind:     global_buffer
      - .actual_access:  write_only
        .address_space:  global
        .offset:         136
        .size:           8
        .value_kind:     global_buffer
    .group_segment_fixed_size: 14400
    .kernarg_segment_align: 8
    .kernarg_segment_size: 144
    .language:       OpenCL C
    .language_version:
      - 2
      - 0
    .max_flat_workgroup_size: 256
    .name:           _Z10prep_all_kPKfS0_S0_S0_S0_S0_PDF16_S1_S1_S1_S1_S1_S0_S0_S0_S0_S1_Pj
    .private_segment_fixed_size: 0
    .sgpr_count:     27
    .sgpr_spill_count: 0
    .symbol:         _Z10prep_all_kPKfS0_S0_S0_S0_S0_PDF16_S1_S1_S1_S1_S1_S0_S0_S0_S0_S1_Pj.kd
    .uniform_work_group_size: 1
    .uses_dynamic_stack: false
    .vgpr_count:     64
    .vgpr_spill_count: 0
    .wavefront_size: 64
  - .agpr_count:     0
    .args:
      - .actual_access:  read_only
        .address_space:  global
        .offset:         0
        .size:           8
        .value_kind:     global_buffer
      - .actual_access:  read_only
        .address_space:  global
        .offset:         8
        .size:           8
        .value_kind:     global_buffer
      - .actual_access:  read_only
        .address_space:  global
        .offset:         16
        .size:           8
        .value_kind:     global_buffer
      - .actual_access:  read_only
        .address_space:  global
        .offset:         24
        .size:           8
        .value_kind:     global_buffer
      - .actual_access:  read_only
        .address_space:  global
        .offset:         32
        .size:           8
        .value_kind:     global_buffer
      - .actual_access:  read_only
        .address_space:  global
        .offset:         40
        .size:           8
        .value_kind:     global_buffer
      - .actual_access:  write_only
        .address_space:  global
        .offset:         48
        .size:           8
        .value_kind:     global_buffer
    .group_segment_fixed_size: 0
    .kernarg_segment_align: 8
    .kernarg_segment_size: 56
    .language:       OpenCL C
    .language_version:
      - 2
      - 0
    .max_flat_workgroup_size: 256
    .name:           _Z9finish6_kPKDF16_PKfS2_S2_S2_S2_Pf
    .private_segment_fixed_size: 0
    .sgpr_count:     18
    .sgpr_spill_count: 0
    .symbol:         _Z9finish6_kPKDF16_PKfS2_S2_S2_S2_Pf.kd
    .uniform_work_group_size: 1
    .uses_dynamic_stack: false
    .vgpr_count:     51
    .vgpr_spill_count: 0
    .wavefront_size: 64
  - .agpr_count:     0
    .args:
      - .actual_access:  read_only
        .address_space:  global
        .offset:         0
        .size:           8
        .value_kind:     global_buffer
      - .actual_access:  write_only
        .address_space:  global
        .offset:         8
        .size:           8
        .value_kind:     global_buffer
    .group_segment_fixed_size: 16640
    .kernarg_segment_align: 8
    .kernarg_segment_size: 16
    .language:       OpenCL C
    .language_version:
      - 2
      - 0
    .max_flat_workgroup_size: 256
    .name:           _Z6gram_kPKfPf
    .private_segment_fixed_size: 0
    .sgpr_count:     16
    .sgpr_spill_count: 0
    .symbol:         _Z6gram_kPKfPf.kd
    .uniform_work_group_size: 1
    .uses_dynamic_stack: false
    .vgpr_count:     38
    .vgpr_spill_count: 0
    .wavefront_size: 64
  - .agpr_count:     0
    .args:
      - .actual_access:  read_only
        .address_space:  global
        .offset:         0
        .size:           8
        .value_kind:     global_buffer
      - .address_space:  global
        .offset:         8
        .size:           8
        .value_kind:     global_buffer
      - .actual_access:  read_only
        .address_space:  global
        .offset:         16
        .size:           8
        .value_kind:     global_buffer
      - .actual_access:  read_only
        .address_space:  global
        .offset:         24
        .size:           8
        .value_kind:     global_buffer
      - .actual_access:  read_only
        .address_space:  global
        .offset:         32
        .size:           8
        .value_kind:     global_buffer
      - .actual_access:  write_only
        .address_space:  global
        .offset:         40
        .size:           8
        .value_kind:     global_buffer
      - .actual_access:  read_only
        .address_space:  global
        .offset:         48
        .size:           8
        .value_kind:     global_buffer
      - .offset:         56
        .size:           4
        .value_kind:     by_value
      - .actual_access:  read_only
        .address_space:  global
        .offset:         64
        .size:           8
        .value_kind:     global_buffer
      - .actual_access:  read_only
        .address_space:  global
        .offset:         72
        .size:           8
        .value_kind:     global_buffer
      - .actual_access:  read_only
        .address_space:  global
        .offset:         80
        .size:           8
        .value_kind:     global_buffer
      - .actual_access:  read_only
        .address_space:  global
        .offset:         88
        .size:           8
        .value_kind:     global_buffer
    .group_segment_fixed_size: 147456
    .kernarg_segment_align: 8
    .kernarg_segment_size: 96
    .language:       OpenCL C
    .language_version:
      - 2
      - 0
    .max_flat_workgroup_size: 512
    .name:           _Z6conv_kILi64ELi128ELi20ELi128ELi4ELi4ELb1EEvPKDF16_S1_PKfS3_PDF16_S4_S1_fS3_S3_S3_S3_
    .private_segment_fixed_size: 0
    .sgpr_count:     43
    .sgpr_spill_count: 0
    .symbol:         _Z6conv_kILi64ELi128ELi20ELi128ELi4ELi4ELb1EEvPKDF16_S1_PKfS3_PDF16_S4_S1_fS3_S3_S3_S3_.kd
    .uniform_work_group_size: 1
    .uses_dynamic_stack: false
    .vgpr_count:     164
    .vgpr_spill_count: 0
    .wavefront_size: 64
  - .agpr_count:     0
    .args:
      - .actual_access:  read_only
        .address_space:  global
        .offset:         0
        .size:           8
        .value_kind:     global_buffer
      - .actual_access:  read_only
        .address_space:  global
        .offset:         8
        .size:           8
        .value_kind:     global_buffer
      - .actual_access:  read_only
        .address_space:  global
        .offset:         16
        .size:           8
        .value_kind:     global_buffer
      - .actual_access:  write_only
        .address_space:  global
        .offset:         24
        .size:           8
        .value_kind:     global_buffer
    .group_segment_fixed_size: 0
    .kernarg_segment_align: 8
    .kernarg_segment_size: 32
    .language:       OpenCL C
    .language_version:
      - 2
      - 0
    .max_flat_workgroup_size: 256
    .name:           _Z8finish_kILi128ELi4EEvPKDF16_PKfS3_PDF16_
    .private_segment_fixed_size: 0
    .sgpr_count:     18
    .sgpr_spill_count: 0
    .symbol:         _Z8finish_kILi128ELi4EEvPKDF16_PKfS3_PDF16_.kd
    .uniform_work_group_size: 1
    .uses_dynamic_stack: false
    .vgpr_count:     44
    .vgpr_spill_count: 0
    .wavefront_size: 64
  - .agpr_count:     0
    .args:
      - .address_space:  global
        .offset:         0
        .size:           8
        .value_kind:     global_buffer
      - .address_space:  global
        .offset:         8
        .size:           8
        .value_kind:     global_buffer
      - .address_space:  global
        .offset:         16
        .size:           8
        .value_kind:     global_buffer
      - .actual_access:  read_only
        .address_space:  global
        .offset:         24
        .size:           8
        .value_kind:     global_buffer
      - .actual_access:  write_only
        .address_space:  global
        .offset:         32
        .size:           8
        .value_kind:     global_buffer
      - .actual_access:  read_only
        .address_space:  global
        .offset:         40
        .size:           8
        .value_kind:     global_buffer
      - .address_space:  global
        .offset:         48
        .size:           8
        .value_kind:     global_buffer
      - .offset:         56
        .size:           4
        .value_kind:     by_value
      - .actual_access:  read_only
        .address_space:  global
        .offset:         64
        .size:           8
        .value_kind:     global_buffer
      - .actual_access:  read_only
        .address_space:  global
        .offset:         72
        .size:           8
        .value_kind:     global_buffer
      - .actual_access:  read_only
        .address_space:  global
        .offset:         80
        .size:           8
        .value_kind:     global_buffer
      - .actual_access:  read_only
        .address_space:  global
        .offset:         88
        .size:           8
        .value_kind:     global_buffer
    .group_segment_fixed_size: 163840
    .kernarg_segment_align: 8
    .kernarg_segment_size: 96
    .language:       OpenCL C
    .language_version:
      - 2
      - 0
    .max_flat_workgroup_size: 512
    .name:           _Z6conv_kILi128ELi256ELi3ELi64ELi1ELi1ELb0EEvPKDF16_S1_PKfS3_PDF16_S4_S1_fS3_S3_S3_S3_
    .private_segment_fixed_size: 0
    .sgpr_count:     51
    .sgpr_spill_count: 0
    .symbol:         _Z6conv_kILi128ELi256ELi3ELi64ELi1ELi1ELb0EEvPKDF16_S1_PKfS3_PDF16_S4_S1_fS3_S3_S3_S3_.kd
    .uniform_work_group_size: 1
    .uses_dynamic_stack: false
    .vgpr_count:     184
    .vgpr_spill_count: 0
    .wavefront_size: 64
  - .agpr_count:     0
    .args:
      - .address_space:  global
        .offset:         0
        .size:           8
        .value_kind:     global_buffer
      - .address_space:  global
        .offset:         8
        .size:           8
        .value_kind:     global_buffer
      - .address_space:  global
        .offset:         16
        .size:           8
        .value_kind:     global_buffer
      - .actual_access:  read_only
        .address_space:  global
        .offset:         24
        .size:           8
        .value_kind:     global_buffer
      - .actual_access:  write_only
        .address_space:  global
        .offset:         32
        .size:           8
        .value_kind:     global_buffer
      - .actual_access:  read_only
        .address_space:  global
        .offset:         40
        .size:           8
        .value_kind:     global_buffer
      - .address_space:  global
        .offset:         48
        .size:           8
        .value_kind:     global_buffer
      - .offset:         56
        .size:           4
        .value_kind:     by_value
      - .actual_access:  read_only
        .address_space:  global
        .offset:         64
        .size:           8
        .value_kind:     global_buffer
      - .actual_access:  read_only
        .address_space:  global
        .offset:         72
        .size:           8
        .value_kind:     global_buffer
      - .actual_access:  read_only
        .address_space:  global
        .offset:         80
        .size:           8
        .value_kind:     global_buffer
      - .actual_access:  read_only
        .address_space:  global
        .offset:         88
        .size:           8
        .value_kind:     global_buffer
    .group_segment_fixed_size: 163840
    .kernarg_segment_align: 8
    .kernarg_segment_size: 96
    .language:       OpenCL C
    .language_version:
      - 2
      - 0
    .max_flat_workgroup_size: 512
    .name:           _Z6conv_kILi256ELi512ELi3ELi128ELi1ELi1ELb0EEvPKDF16_S1_PKfS3_PDF16_S4_S1_fS3_S3_S3_S3_
    .private_segment_fixed_size: 0
    .sgpr_count:     64
    .sgpr_spill_count: 0
    .symbol:         _Z6conv_kILi256ELi512ELi3ELi128ELi1ELi1ELb0EEvPKDF16_S1_PKfS3_PDF16_S4_S1_fS3_S3_S3_S3_.kd
    .uniform_work_group_size: 1
    .uses_dynamic_stack: false
    .vgpr_count:     184
    .vgpr_spill_count: 0
    .wavefront_size: 64
  - .agpr_count:     0
    .args:
      - .address_space:  global
        .offset:         0
        .size:           8
        .value_kind:     global_buffer
      - .address_space:  global
        .offset:         8
        .size:           8
        .value_kind:     global_buffer
      - .address_space:  global
        .offset:         16
        .size:           8
        .value_kind:     global_buffer
      - .actual_access:  read_only
        .address_space:  global
        .offset:         24
        .size:           8
        .value_kind:     global_buffer
      - .actual_access:  write_only
        .address_space:  global
        .offset:         32
        .size:           8
        .value_kind:     global_buffer
      - .actual_access:  read_only
        .address_space:  global
        .offset:         40
        .size:           8
        .value_kind:     global_buffer
      - .address_space:  global
        .offset:         48
        .size:           8
        .value_kind:     global_buffer
      - .offset:         56
        .size:           4
        .value_kind:     by_value
      - .actual_access:  read_only
        .address_space:  global
        .offset:         64
        .size:           8
        .value_kind:     global_buffer
      - .actual_access:  read_only
        .address_space:  global
        .offset:         72
        .size:           8
        .value_kind:     global_buffer
      - .actual_access:  read_only
        .address_space:  global
        .offset:         80
        .size:           8
        .value_kind:     global_buffer
      - .actual_access:  read_only
        .address_space:  global
        .offset:         88
        .size:           8
        .value_kind:     global_buffer
    .group_segment_fixed_size: 163840
    .kernarg_segment_align: 8
    .kernarg_segment_size: 96
    .language:       OpenCL C
    .language_version:
      - 2
      - 0
    .max_flat_workgroup_size: 512
    .name:           _Z6conv_kILi512ELi256ELi3ELi64ELi1ELi1ELb0EEvPKDF16_S1_PKfS3_PDF16_S4_S1_fS3_S3_S3_S3_
    .private_segment_fixed_size: 0
    .sgpr_count:     66
    .sgpr_spill_count: 0
    .symbol:         _Z6conv_kILi512ELi256ELi3ELi64ELi1ELi1ELb0EEvPKDF16_S1_PKfS3_PDF16_S4_S1_fS3_S3_S3_S3_.kd
    .uniform_work_group_size: 1
    .uses_dynamic_stack: false
    .vgpr_count:     204
    .vgpr_spill_count: 0
    .wavefront_size: 64
  - .agpr_count:     0
    .args:
      - .address_space:  global
        .offset:         0
        .size:           8
        .value_kind:     global_buffer
      - .address_space:  global
        .offset:         8
        .size:           8
        .value_kind:     global_buffer
      - .actual_access:  read_only
        .address_space:  global
        .offset:         16
        .size:           8
        .value_kind:     global_buffer
      - .actual_access:  read_only
        .address_space:  global
        .offset:         24
        .size:           8
        .value_kind:     global_buffer
      - .actual_access:  read_only
        .address_space:  global
        .offset:         32
        .size:           8
        .value_kind:     global_buffer
      - .actual_access:  write_only
        .address_space:  global
        .offset:         40
        .size:           8
        .value_kind:     global_buffer
      - .address_space:  global
        .offset:         48
        .size:           8
        .value_kind:     global_buffer
      - .offset:         56
        .size:           4
        .value_kind:     by_value
      - .actual_access:  read_only
        .address_space:  global
        .offset:         64
        .size:           8
        .value_kind:     global_buffer
      - .actual_access:  read_only
        .address_space:  global
        .offset:         72
        .size:           8
        .value_kind:     global_buffer
      - .actual_access:  read_only
        .address_space:  global
        .offset:         80
        .size:           8
        .value_kind:     global_buffer
      - .actual_access:  read_only
        .address_space:  global
        .offset:         88
        .size:           8
        .value_kind:     global_buffer
    .group_segment_fixed_size: 163840
    .kernarg_segment_align: 8
    .kernarg_segment_size: 96
    .language:       OpenCL C
    .language_version:
      - 2
      - 0
    .max_flat_workgroup_size: 512
    .name:           _Z6conv_kILi256ELi128ELi3ELi64ELi1ELi2ELb0EEvPKDF16_S1_PKfS3_PDF16_S4_S1_fS3_S3_S3_S3_
    .private_segment_fixed_size: 0
    .sgpr_count:     55
    .sgpr_spill_count: 0
    .symbol:         _Z6conv_kILi256ELi128ELi3ELi64ELi1ELi2ELb0EEvPKDF16_S1_PKfS3_PDF16_S4_S1_fS3_S3_S3_S3_.kd
    .uniform_work_group_size: 1
    .uses_dynamic_stack: false
    .vgpr_count:     172
    .vgpr_spill_count: 0
    .wavefront_size: 64
  - .agpr_count:     0
    .args:
      - .actual_access:  read_only
        .address_space:  global
        .offset:         0
        .size:           8
        .value_kind:     global_buffer
      - .actual_access:  read_only
        .address_space:  global
        .offset:         8
        .size:           8
        .value_kind:     global_buffer
      - .actual_access:  read_only
        .address_space:  global
        .offset:         16
        .size:           8
        .value_kind:     global_buffer
      - .actual_access:  write_only
        .address_space:  global
        .offset:         24
        .size:           8
        .value_kind:     global_buffer
    .group_segment_fixed_size: 0
    .kernarg_segment_align: 8
    .kernarg_segment_size: 32
    .language:       OpenCL C
    .language_version:
      - 2
      - 0
    .max_flat_workgroup_size: 256
    .name:           _Z8finish_kILi128ELi2EEvPKDF16_PKfS3_PDF16_
    .private_segment_fixed_size: 0
    .sgpr_count:     18
    .sgpr_spill_count: 0
    .symbol:         _Z8finish_kILi128ELi2EEvPKDF16_PKfS3_PDF16_.kd
    .uniform_work_group_size: 1
    .uses_dynamic_stack: false
    .vgpr_count:     28
    .vgpr_spill_count: 0
    .wavefront_size: 64
  - .agpr_count:     0
    .args:
      - .address_space:  global
        .offset:         0
        .size:           8
        .value_kind:     global_buffer
      - .address_space:  global
        .offset:         8
        .size:           8
        .value_kind:     global_buffer
      - .actual_access:  read_only
        .address_space:  global
        .offset:         16
        .size:           8
        .value_kind:     global_buffer
      - .actual_access:  read_only
        .address_space:  global
        .offset:         24
        .size:           8
        .value_kind:     global_buffer
      - .actual_access:  read_only
        .address_space:  global
        .offset:         32
        .size:           8
        .value_kind:     global_buffer
      - .actual_access:  write_only
        .address_space:  global
        .offset:         40
        .size:           8
        .value_kind:     global_buffer
      - .address_space:  global
        .offset:         48
        .size:           8
        .value_kind:     global_buffer
      - .offset:         56
        .size:           4
        .value_kind:     by_value
      - .actual_access:  read_only
        .address_space:  global
        .offset:         64
        .size:           8
        .value_kind:     global_buffer
      - .actual_access:  read_only
        .address_space:  global
        .offset:         72
        .size:           8
        .value_kind:     global_buffer
      - .actual_access:  read_only
        .address_space:  global
        .offset:         80
        .size:           8
        .value_kind:     global_buffer
      - .actual_access:  read_only
        .address_space:  global
        .offset:         88
        .size:           8
        .value_kind:     global_buffer
    .group_segment_fixed_size: 147456
    .kernarg_segment_align: 8
    .kernarg_segment_size: 96
    .language:       OpenCL C
    .language_version:
      - 2
      - 0
    .max_flat_workgroup_size: 512
    .name:           _Z6conv_kILi128ELi64ELi20ELi64ELi4ELi4ELb0EEvPKDF16_S1_PKfS3_PDF16_S4_S1_fS3_S3_S3_S3_
    .private_segment_fixed_size: 0
    .sgpr_count:     64
    .sgpr_spill_count: 0
    .symbol:         _Z6conv_kILi128ELi64ELi20ELi64ELi4ELi4ELb0EEvPKDF16_S1_PKfS3_PDF16_S4_S1_fS3_S3_S3_S3_.kd
    .uniform_work_group_size: 1
    .uses_dynamic_stack: false
    .vgpr_count:     184
    .vgpr_spill_count: 0
    .wavefront_size: 64
